# grid barrier after the prologue replaced by a 32-producer flag: each workgroup starts the first pre-norm as soon as layer-0 adaLN shift/scale are published
# speedup vs baseline: 1.0233x; 1.0233x over previous
; #define LAS __attribute__((address_space(3)))
; DI kptr_t kargs_now() { kptr_t p = (kptr_t)__builtin_amdgcn_kernarg_segment_ptr(); asm volatile("" : "+s"(p)); return p; }
; DI const float* inp(kptr_t k, int i) { return (const float*)k[i]; }
; DI void refresh(Frame& F) { int w = F.wave; unsigned ones_ = ~0u; asm volatile("" : "+s"(w), "+s"(ones_)); int ln = (int)__builtin_amdgcn_mbcnt_hi(ones_, __builtin_amdgcn_mbcnt_lo(ones_, 0u)); asm volatile("" : "+v"(ln)); F.tid = w * 64 + ln; F.lane = ln; F.wave = w; int b = blockIdx.x; asm volatile("" : "+s"(b)); F.bid = b; }
; DI void p_adaln_unit(Frame& F, int unit) {
;     ...
;     __syncthreads();
;     float* mod = (float*)(F.ws + WS_MOD);
;     for (int o = F.tid; o < 1024; o += 512) { const int b = o >> 6, col = o & 63; float s = inp(KA, I_BADA)[(size_t)l * NMOD * D + cb * 64 + col];
; #pragma unroll
;         for (int w = 0; w < 8; ++w) s += part[(w * 16 + b) * 64 + col];
;         mod[((size_t)l * NB + b) * (NMOD * D) + cb * 64 + col] = s; }
;     __syncthreads();
; DI void p_ssm_unit(Frame& F, int unit) {
;     refresh(F);
;     const kptr_t KA = kargs_now();
;     const int l = unit / NG, g = unit % NG;
;     LAS double* Lp = (LAS double*)F.lds;
;     LAS float* Bb = (LAS float*)(F.lds + 33792);
;     LAS float* Cc = (LAS float*)(F.lds + 50176);
;     LAS float* Kt = (LAS float*)(F.lds + 66560);
;     const int lg = l * NG + g;
;     const double dt = exp_d((double)inp(KA, I_LOGDT)[lg]);
;     for (int i = F.tid; i < 33 * 64; i += 512) { const int tau = i >> 6, p = i & 63;
;         const double lre = fmin((double)inp(KA, I_ARE)[lg * SP + p], -1e-4), lim = (double)inp(KA, I_AIM)[lg * SP + p];
;         const double mag = exp_d(lre * dt * (double)tau); double sn, cs; sincos_d(lim * dt * (double)tau, sn, cs);
;         Lp[i * 2] = mag * cs; Lp[i * 2 + 1] = mag * sn; }
.LBB0_16:
	s_or_b64 exec, exec, s[10:11]
	s_mov_b64 s[4:5], 0
	s_barrier
	s_cmp_lt_u32 s88, 64
	s_cbranch_scc1 .Lsig_skip
	s_cmp_gt_u32 s88, 95
	s_cbranch_scc1 .Lsig_skip
	s_waitcnt vmcnt(0)
	s_barrier
	s_cmp_lg_u32 s97, 0
	s_cbranch_scc1 .Lsig_skip
	v_readlane_b32 s100, v253, 10
	v_readlane_b32 s101, v253, 11
	s_mov_b64 s[6:7], exec
	s_mov_b64 exec, 1
	s_add_u32 s100, s100, 0xc000
	s_addc_u32 s101, s101, 0
	buffer_wbl2 sc1
	s_waitcnt vmcnt(0)
	v_mov_b32_e32 v2, 0
	v_mov_b32_e32 v3, 1
	global_atomic_add v2, v3, s[100:101]
	s_waitcnt vmcnt(0)
	s_mov_b64 exec, s[6:7]
.Lsig_skip:
.LBB0_17:
	s_and_b64 vcc, exec, s[4:5]
	s_cbranch_vccz .LBB0_76
	s_mov_b32 s97, s12
	s_mov_b32 s4, -1
	s_lshl_b32 s44, s97, 6
	v_mbcnt_lo_u32_b32 v0, s4, 0
	v_mbcnt_hi_u32_b32 v20, s4, v0
	v_readlane_b32 s4, v253, 29
	v_readlane_b32 s5, v253, 30
	v_add_u32_e32 v10, s44, v20
	s_mov_b32 s14, 0x6dc9c883
	v_readlane_b32 s90, v253, 6
	s_movk_i32 s4, 0x840
	s_mov_b32 s15, 0x3fc45f30
	v_readlane_b32 s91, v253, 7
	s_ashr_i32 s89, s88, 31
	v_cmp_gt_i32_e64 s[4:5], s4, v10
	s_and_saveexec_b64 s[6:7], s[4:5]
	s_cbranch_execz .LBB0_21
	s_load_dwordx2 s[8:9], s[90:91], 0x60
	s_lshl_b64 s[10:11], s[88:89], 2
	s_mov_b32 s70, s18
	s_mov_b32 s72, s16
	s_mov_b32 s74, s20
	s_waitcnt lgkmcnt(0)
	s_add_u32 s8, s8, s10
	s_addc_u32 s9, s9, s11
	global_load_dword v4, v9, s[8:9]
	s_load_dwordx4 s[8:11], s[90:91], 0x50
	s_lshl_b32 s12, s88, 6
	v_and_or_b32 v0, v20, 63, s12
	v_ashrrev_i32_e32 v1, 31, v0
	v_lshlrev_b64 v[0:1], 2, v[0:1]
	s_waitcnt lgkmcnt(0)
	v_lshl_add_u64 v[2:3], s[8:9], 0, v[0:1]
	v_lshl_add_u64 v[0:1], s[10:11], 0, v[0:1]
	global_load_dword v11, v[2:3], off
	global_load_dword v21, v[0:1], off
	s_mov_b32 s76, s22
	s_mov_b32 s78, s18
	s_mov_b32 s80, s16
	s_mov_b32 s82, s20
	s_mov_b32 s84, s28
	s_lshl_b32 s10, s97, 10
	s_add_i32 s10, s10, 0
	s_mov_b64 s[8:9], 0
	v_lshl_add_u32 v8, v20, 4, s10
	s_waitcnt vmcnt(2)
	v_cvt_f64_f32_e32 v[0:1], v4
	v_mul_f64 v[2:3], v[0:1], s[0:1]
	v_rndne_f64_e32 v[2:3], v[2:3]
	v_fmac_f64_e32 v[0:1], s[2:3], v[2:3]
	v_cvt_i32_f64_e32 v24, v[2:3]
	v_add_f64 v[2:3], v[0:1], 1.0
	v_mul_f64 v[4:5], v[0:1], 0.5
	v_mul_f64 v[6:7], v[0:1], s[16:17]
	v_mul_f64 v[46:47], v[0:1], v[4:5]
	v_fmac_f64_e32 v[2:3], v[0:1], v[4:5]
	v_ldexp_f64 v[12:13], v[0:1], -2
	v_mul_f64 v[4:5], v[6:7], v[46:47]
	v_fmac_f64_e32 v[2:3], v[6:7], v[46:47]
	v_mul_f64 v[14:15], v[0:1], s[70:71]
	v_mul_f64 v[6:7], v[12:13], v[4:5]
	v_fmac_f64_e32 v[2:3], v[12:13], v[4:5]
	v_mul_f64 v[16:17], v[0:1], s[72:73]
	v_mul_f64 v[4:5], v[14:15], v[6:7]
	v_fmac_f64_e32 v[2:3], v[14:15], v[6:7]
	v_mul_f64 v[18:19], v[0:1], s[74:75]
	v_mul_f64 v[6:7], v[16:17], v[4:5]
	v_fmac_f64_e32 v[2:3], v[16:17], v[4:5]
	v_ldexp_f64 v[22:23], v[0:1], -3
	v_mul_f64 v[4:5], v[18:19], v[6:7]
	v_fmac_f64_e32 v[2:3], v[18:19], v[6:7]
	v_mul_f64 v[26:27], v[0:1], s[76:77]
	v_mul_f64 v[6:7], v[22:23], v[4:5]
	v_fmac_f64_e32 v[2:3], v[22:23], v[4:5]
	v_mul_f64 v[28:29], v[0:1], s[78:79]
	v_mul_f64 v[4:5], v[26:27], v[6:7]
	v_fmac_f64_e32 v[2:3], v[26:27], v[6:7]
	v_mul_f64 v[30:31], v[0:1], s[24:25]
	v_mul_f64 v[6:7], v[28:29], v[4:5]
	v_fmac_f64_e32 v[2:3], v[28:29], v[4:5]
	v_mul_f64 v[32:33], v[0:1], s[80:81]
	v_mul_f64 v[4:5], v[30:31], v[6:7]
	v_fmac_f64_e32 v[2:3], v[30:31], v[6:7]
	v_mul_f64 v[34:35], v[0:1], s[26:27]
	v_mul_f64 v[6:7], v[32:33], v[4:5]
	v_fmac_f64_e32 v[2:3], v[32:33], v[4:5]
	v_mul_f64 v[36:37], v[0:1], s[82:83]
	v_mul_f64 v[4:5], v[34:35], v[6:7]
	v_fmac_f64_e32 v[2:3], v[34:35], v[6:7]
	v_mul_f64 v[38:39], v[0:1], s[84:85]
	v_mul_f64 v[6:7], v[36:37], v[4:5]
	v_fmac_f64_e32 v[2:3], v[36:37], v[4:5]
	v_ldexp_f64 v[40:41], v[0:1], -4
	v_mul_f64 v[4:5], v[38:39], v[6:7]
	v_fmac_f64_e32 v[2:3], v[38:39], v[6:7]
	s_waitcnt vmcnt(1)
	v_cvt_f64_f32_e32 v[42:43], v11
	v_fmac_f64_e32 v[2:3], v[40:41], v[4:5]
	s_waitcnt vmcnt(0)
	v_cvt_f64_f32_e32 v[44:45], v21
	v_min_f64 v[0:1], v[42:43], s[30:31]
	v_ldexp_f64 v[2:3], v[2:3], v24
	v_mul_f64 v[0:1], v[0:1], v[2:3]
	v_mul_f64 v[2:3], v[2:3], v[44:45]
	v_mov_b32_e32 v11, v10

; DI void p_transposes(Frame& F) { refresh(F); QState q; q.base = 0; q.cnt = 8; run_items1(F, 0, -1, q); }
; #define REP(k) for (int _r = 0; _r < ((DUP_PHASE == (k)) ? 2 : 1); ++_r)
; #define GRID_BAR() do { XcdBarrier _b = bar; asm volatile("" : "+s"(_b.bar), "+s"(_b.x)); refresh(F); xcd_barrier(_b, F.tid == 0); } while (0)
; __device__ __forceinline__ void xcd_barrier(const XcdBarrier& b, bool t0) {
;     asm volatile("s_waitcnt vmcnt(0)" ::: "memory");
;     __syncthreads();
;     if (t0) {
;         unsigned* bar = b.bar;
;         __builtin_amdgcn_s_waitcnt(0);
;         unsigned nloc = b.st[0], nx = b.st[1];
;         if (nloc == 0u) { xcd_barrier_complete(bar, b.x, nloc, nx); b.st[0] = nloc; b.st[1] = nx; }
; __global__ void __launch_bounds__(512, 2) fwd_kernel(Args args) {
;     ...
;     REP(1) { for (int u = F.bid; u < 256; u += F.G) { if (u < 64) p_ssm_unit(F, u); else p_adaln_unit(F, u - 64); }
;     p_transposes(F); __syncthreads(); }
;     GRID_BAR();
.LBB0_124:
	v_readlane_b32 s0, v253, 2
	s_mov_b32 s33, s94
	v_readlane_b32 s1, v253, 3
	s_mov_b32 s2, -1
	s_waitcnt lgkmcnt(0)
	s_barrier
	s_mov_b32 s3, s88
	s_waitcnt vmcnt(14)
	v_mbcnt_lo_u32_b32 v0, s2, 0
	v_mbcnt_hi_u32_b32 v0, s2, v0
	s_lshl_b32 s2, s97, 6
	s_waitcnt vmcnt(0)
	s_sub_i32 s2, 0, s2
	v_cmp_eq_u32_e32 vcc, s2, v0
	s_barrier
	s_and_saveexec_b64 s[2:3], vcc
	s_xor_b64 s[2:3], exec, s[2:3]
	s_cbranch_execz .LBB0_178
	v_readlane_b32 s100, v253, 10
	v_readlane_b32 s101, v253, 11
	s_nop 4
	s_add_u32 s100, s100, 0xc000
	s_addc_u32 s101, s101, 0
	v_mov_b32_e32 v2, 0
.Lflag_spin:
	s_sleep 1
	global_load_dword v0, v2, s[100:101] sc1
	s_waitcnt vmcnt(0)
	v_readfirstlane_b32 s4, v0
	s_nop 3
	s_cmp_lt_u32 s4, 32
	s_cbranch_scc1 .Lflag_spin
	buffer_inv sc1
	s_waitcnt vmcnt(0)
	s_branch .LBB0_178
	s_add_i32 s4, 0, 0x20000
	v_mov_b32_e32 v0, s4
	s_waitcnt vmcnt(0) expcnt(0) lgkmcnt(0)
	ds_read_b32 v2, v0
	s_add_i32 s4, 0, 0x20004
	v_mov_b32_e32 v0, s4
	ds_read_b32 v0, v0
	s_waitcnt lgkmcnt(1)
	v_cmp_ne_u32_e32 vcc, 0, v2
	s_cbranch_vccnz .LBB0_141
	v_readlane_b32 s6, v253, 0
	v_readlane_b32 s7, v253, 1
	s_load_dwordx2 s[4:5], s[6:7], 0x4
	s_add_u32 s6, s0, 0x1000
	s_addc_u32 s7, s1, 0
	s_add_u32 s8, s0, 0x1100
	s_addc_u32 s9, s1, 0
	s_add_u32 s10, s0, 0x1200
	s_addc_u32 s11, s1, 0
	s_add_u32 s12, s0, 0x1300
	s_waitcnt lgkmcnt(0)
	s_mul_i32 s22, s4, s72
	s_addc_u32 s13, s1, 0
	s_mul_i32 s22, s22, s5
	s_mov_b32 s23, 1
	s_mov_b64 s[4:5], 0
	v_mov_b64_e32 v[0:1], s[0:1]
	v_mov_b64_e32 v[2:3], s[6:7]
	v_mov_b64_e32 v[4:5], s[8:9]
	v_mov_b64_e32 v[6:7], s[10:11]
	v_mov_b64_e32 v[8:9], s[12:13]
	s_branch .LBB0_129
